# k_gcn: layer-2 weight fragments loaded at gather-loop exit instead of kernel start
# baseline (speedup 1.0000x reference)
_Z5k_gcnILi128ELb1ELi16EEvPKDv8_DF16_PKiS4_PKfS2_S6_PDF16_S6_S6_S2_S6_S2_S6_S6_S6_PfS4_:
	s_load_dwordx4 s[20:23], s[0:1], 0x8
	s_load_dwordx2 s[4:5], s[0:1], 0x20
	v_readfirstlane_b32 s30, v0
	v_and_b32_e32 v1, 63, v0
	s_lshr_b32 s28, s30, 6
	v_lshl_or_b32 v2, s28, 9, v1
	v_mov_b32_e32 v3, 0
	v_bfe_u32 v83, v0, 4, 2
	s_waitcnt lgkmcnt(0)
	v_lshl_add_u64 v[14:15], v[2:3], 4, s[4:5]
	v_ashrrev_i32_e32 v3, 31, v2
	s_lshl_b32 s29, s2, 4
	s_lshl_b32 s6, s28, 2
	v_or_b32_e32 v38, s29, v83
	v_add_lshl_u32 v38, v38, s6, 2
	global_load_dwordx2 v[50:51], v38, s[20:21]
	v_lshl_add_u64 v[16:17], v[2:3], 4, s[4:5]
	v_or_b32_e32 v14, s29, v83
	s_lshl_b32 s6, s28, 2
	v_add_u32_e32 v14, s6, v14
	s_movk_i32 s3, 0x1000
	v_ashrrev_i32_e32 v15, 31, v14
	v_add_co_u32_e32 v34, vcc, s3, v16
	v_lshl_add_u64 v[36:37], v[14:15], 2, s[20:21]
	s_nop 0
	v_addc_co_u32_e32 v35, vcc, 0, v17, vcc
	s_waitcnt vmcnt(0)
	v_sub_u32_e32 v53, v51, v50
	v_lshlrev_b32_e32 v34, 2, v50
	global_load_dword v36, v34, s[22:23]
	global_load_dword v38, v34, s[22:23] offset:4
	global_load_dword v42, v34, s[22:23] offset:8
	global_load_dword v46, v34, s[22:23] offset:12
	s_load_dwordx2 s[24:25], s[0:1], 0x0
	s_load_dwordx2 s[2:3], s[0:1], 0x18
	v_and_b32_e32 v82, 15, v0
	v_or_b32_e32 v51, s6, v83
	v_add_u32_e32 v34, s29, v51
	v_lshlrev_b32_e32 v54, 4, v82
	s_mov_b32 s27, 0x20000
	s_mov_b32 s26, 0x4e2100
	s_waitcnt lgkmcnt(0)
	s_and_b32 s25, s25, 0xffff
	v_lshl_or_b32 v35, v34, 8, v54
	buffer_load_dwordx4 v[64:67], v35, s[24:27], 0 offen
	v_ashrrev_i32_e32 v35, 31, v34
	v_lshl_add_u64 v[34:35], v[34:35], 2, s[2:3]
	global_load_dword v52, v[34:35], off
	v_mbcnt_lo_u32_b32 v34, -1, 0
	v_mbcnt_hi_u32_b32 v34, -1, v34
	v_and_b32_e32 v37, 64, v34
	v_xor_b32_e32 v35, 32, v34
	v_add_u32_e32 v37, 64, v37
	v_cmp_lt_i32_e32 vcc, v35, v37
	v_xor_b32_e32 v39, 16, v34
	s_load_dwordx2 s[2:3], s[0:1], 0x78
	s_load_dwordx8 s[4:11], s[0:1], 0x58
	s_load_dwordx8 s[12:19], s[0:1], 0x38
	v_cndmask_b32_e32 v35, v34, v35, vcc
	v_lshlrev_b32_e32 v84, 2, v35
	ds_bpermute_b32 v35, v84, v53
	v_cmp_lt_i32_e32 vcc, v39, v37
	s_mov_b32 s33, 4
	s_waitcnt vmcnt(1)
	v_mov_b32_e32 v70, 0x4e20
	v_cmp_lt_i32_e64 s[34:35], 0, v53
	v_cmp_lt_i32_e64 s[36:37], 1, v53
	v_cmp_lt_i32_e64 s[38:39], 2, v53
	v_cmp_lt_i32_e64 s[40:41], 3, v53
	v_cndmask_b32_e64 v36, v70, v36, s[34:35]
	v_cndmask_b32_e64 v38, v70, v38, s[36:37]
	v_cndmask_b32_e64 v42, v70, v42, s[38:39]
	v_cndmask_b32_e64 v46, v70, v46, s[40:41]
	v_cvt_f32_f16_e32 v62, v64
	v_cndmask_b32_e32 v34, v34, v39, vcc
	v_lshlrev_b32_e32 v85, 2, v34
	s_waitcnt lgkmcnt(0)
	v_max_i32_e32 v34, v53, v35
	ds_bpermute_b32 v35, v85, v34
	v_cvt_f32_f16_sdwa v63, v64 dst_sel:DWORD dst_unused:UNUSED_PAD src0_sel:WORD_1
	v_cvt_f32_f16_e32 v60, v65
	v_cvt_f32_f16_sdwa v61, v65 dst_sel:DWORD dst_unused:UNUSED_PAD src0_sel:WORD_1
	v_cvt_f32_f16_e32 v58, v66
	v_cvt_f32_f16_sdwa v59, v66 dst_sel:DWORD dst_unused:UNUSED_PAD src0_sel:WORD_1
	v_cvt_f32_f16_e32 v56, v67
	v_cvt_f32_f16_sdwa v57, v67 dst_sel:DWORD dst_unused:UNUSED_PAD src0_sel:WORD_1
	s_waitcnt lgkmcnt(0)
	v_max_i32_e32 v34, v34, v35
	s_nop 0
	v_readfirstlane_b32 s31, v34
	s_cmp_lt_i32 s31, 1
	s_cbranch_scc1 .LBB2_19

.LBB2_19:
	s_load_dwordx2 s[34:35], s[0:1], 0x20
	s_load_dwordx2 s[0:1], s[0:1], 0x28
	v_mov_b32_e32 v35, 0
	v_lshlrev_b32_e32 v34, 4, v83
	s_lshl_b32 s20, s28, 5
	s_mov_b32 s21, 0
	s_waitcnt lgkmcnt(0)
	v_lshl_add_u64 v[36:37], s[0:1], 0, v[34:35]
	v_lshl_add_u64 v[36:37], s[20:21], 2, v[36:37]
	global_load_dwordx4 v[70:73], v[36:37], off
	global_load_dwordx4 v[74:77], v[36:37], off offset:64
	v_mov_b32_e32 v36, v63
	v_mov_b32_e32 v37, v60
	s_waitcnt vmcnt(2)
	s_lshl_b32 s36, s28, 13
	v_lshl_add_u32 v64, v1, 4, s36
	v_add_u32_e32 v65, 0x1000, v64
	global_load_dwordx4 v[26:29], v64, s[34:35]
	global_load_dwordx4 v[10:13], v64, s[34:35] offset:1024
	global_load_dwordx4 v[6:9], v64, s[34:35] offset:2048
	global_load_dwordx4 v[2:5], v64, s[34:35] offset:3072
	global_load_dwordx4 v[30:33], v65, s[34:35]
	global_load_dwordx4 v[22:25], v65, s[34:35] offset:1024
	global_load_dwordx4 v[18:21], v65, s[34:35] offset:2048
	global_load_dwordx4 v[14:17], v65, s[34:35] offset:3072
	v_pk_mul_f32 v[36:37], v[52:53], v[36:37] op_sel_hi:[0,1]
	v_mov_b32_e32 v38, v61
	v_mov_b32_e32 v39, v58
	v_fma_mixlo_f16 v34, v52, v62, 0
	v_cvt_pk_f16_f32 v37, v36, v37
	v_pk_mul_f32 v[38:39], v[52:53], v[38:39] op_sel_hi:[0,1]
	v_pack_b32_f16 v36, v34, v37
	v_cvt_pk_f16_f32 v34, v38, v39
	v_mov_b32_e32 v38, v59
	v_mov_b32_e32 v39, v56
	v_pk_mul_f32 v[38:39], v[52:53], v[38:39] op_sel_hi:[0,1]
	v_cvt_pk_f16_f32 v39, v38, v39
	s_movk_i32 s20, 0x110
	v_alignbit_b32 v38, v39, v34, 16
	v_lshrrev_b32_e32 v39, 16, v39
	v_mad_u64_u32 v[40:41], s[0:1], v51, s20, v[54:55]
	v_alignbit_b32 v37, v34, v37, 16
	v_fma_mixhi_f16 v39, v52, v57, 0
	v_lshlrev_b32_e32 v86, 2, v83
	v_cmp_gt_u32_e32 vcc, 16, v0
	v_mov_b32_e32 v87, 0
	v_mov_b32_e32 v88, 0
	v_mov_b32_e32 v89, 0
	ds_write_b128 v40, v[36:39] offset:5376
	s_and_saveexec_b64 s[0:1], vcc
	s_cbranch_execz .LBB2_21
	v_or_b32_e32 v36, s29, v0
	v_ashrrev_i32_e32 v37, 31, v36
	s_movk_i32 s21, 0x108
	v_mov_b64_e32 v[38:39], s[12:13]
	v_mad_i64_i32 v[38:39], s[12:13], v36, s21, v[38:39]
	v_lshl_add_u64 v[36:37], v[36:37], 2, s[14:15]
	global_load_dwordx2 v[38:39], v[38:39], off
	s_nop 0
	global_load_dword v34, v[36:37], off
	s_waitcnt vmcnt(1)
	s_waitcnt vmcnt(0)
	v_max_f32_e32 v36, 0, v38
	v_max_f32_e32 v37, 0, v39
	v_max_f32_e32 v34, 0, v34
	v_cvt_f16_f32_e32 v88, v36
	v_cvt_f16_f32_e32 v87, v34
	v_cvt_f16_f32_e32 v89, v37
.LBB2_21:
	s_or_b64 exec, exec, s[0:1]
	s_mul_i32 s0, s28, 0x140
	v_or_b32_e32 v34, s0, v1
	s_add_i32 s1, s0, 64
	v_lshl_add_u64 v[36:37], v[34:35], 4, s[16:17]
	v_or_b32_e32 v34, s1, v1
	s_add_i32 s1, s0, 0x80
	v_lshl_add_u64 v[38:39], v[34:35], 4, s[16:17]
	v_or_b32_e32 v34, s1, v1
	s_add_i32 s1, s0, 0xc0
	global_load_dwordx4 v[54:57], v[36:37], off
	global_load_dwordx4 v[58:61], v[38:39], off
	v_lshl_add_u64 v[36:37], v[34:35], 4, s[16:17]
	v_or_b32_e32 v34, s1, v1
	s_addk_i32 s0, 0x100
	v_lshl_add_u64 v[38:39], v[34:35], 4, s[16:17]
	v_or_b32_e32 v34, s0, v1
	v_lshl_add_u64 v[34:35], v[34:35], 4, s[16:17]
	global_load_dwordx4 v[66:69], v[36:37], off
	global_load_dwordx4 v[62:65], v[38:39], off
	global_load_dwordx4 v[46:49], v[34:35], off
	v_lshl_or_b32 v34, s28, 7, v1
	v_ashrrev_i32_e32 v35, 31, v34
	v_lshl_add_u64 v[34:35], v[34:35], 4, s[4:5]
	s_lshl_b32 s4, s28, 4
	s_lshl_b32 s5, s28, 6
	s_add_u32 s0, s18, s5
	s_addc_u32 s1, s19, 0
	s_add_u32 s6, s6, s5
	global_load_dwordx4 v[38:41], v[34:35], off
	global_load_dwordx4 v[42:45], v[34:35], off offset:1024
	v_lshlrev_b32_e32 v34, 2, v86
	s_addc_u32 s7, s7, 0
	global_load_dwordx4 v[78:81], v34, s[0:1]
	global_load_dwordx4 v[50:53], v34, s[6:7]
	s_add_u32 s0, s8, s5
	s_addc_u32 s1, s9, 0
	global_load_dwordx4 v[34:37], v34, s[0:1]
	v_and_b32_e32 v90, 48, v0
	v_mad_u32_u24 v91, v82, s20, v90
	s_waitcnt lgkmcnt(0)
	s_barrier
	ds_read_b128 v[92:95], v91 offset:5376
	s_waitcnt vmcnt(10) lgkmcnt(0)
	v_mfma_f32_16x16x32_f16 v[26:29], v[26:29], v[92:95], v[70:73]
	s_nop 2
	ds_read_b128 v[70:73], v91 offset:5440
	s_andn2_b32 s30, s30, 63
	s_waitcnt vmcnt(10)
	v_mfma_f32_16x16x32_f16 v[30:33], v[30:33], v[92:95], v[74:77]
	s_nop 2
	ds_read_b128 v[74:77], v91 offset:5568
	s_waitcnt lgkmcnt(1)
	v_mfma_f32_16x16x32_f16 v[10:13], v[10:13], v[70:73], v[26:29]
	s_nop 2
	ds_read_b128 v[26:29], v91 offset:5504
	s_waitcnt lgkmcnt(0)
	v_mfma_f32_16x16x32_f16 v[8:11], v[6:9], v[26:29], v[10:13]
	v_mul_u32_u24_e32 v6, 0x150, v82
	v_mfma_f32_16x16x32_f16 v[2:5], v[2:5], v[74:77], v[8:11]
	s_nop 7
	v_max_f32_e32 v7, 0, v2
	v_max_f32_e32 v8, 0, v3
	v_max_f32_e32 v9, 0, v4
	v_max_f32_e32 v10, v5, v5
	v_mfma_f32_16x16x32_f16 v[2:5], v[22:25], v[70:73], v[30:33]
	v_max_f32_e32 v10, 0, v10
	v_cvt_pk_f16_f32 v9, v9, v10
	v_cvt_pk_f16_f32 v8, v7, v8
	v_mfma_f32_16x16x32_f16 v[2:5], v[18:21], v[26:29], v[2:5]
	v_lshlrev_b32_e32 v7, 3, v83
	v_add3_u32 v7, v6, s30, v7
	v_mfma_f32_16x16x32_f16 v[2:5], v[14:17], v[74:77], v[2:5]
	s_nop 7
	v_max_f32_e32 v10, 0, v3
	v_max_f32_e32 v3, v4, v4
	v_max_f32_e32 v2, 0, v2
	v_max_f32_e32 v3, 0, v3
	v_max_f32_e32 v4, 0, v5
	v_cvt_pk_f16_f32 v3, v3, v4
	v_cvt_pk_f16_f32 v2, v2, v10
	ds_write2_b64 v7, v[8:9], v[2:3] offset1:4
	s_and_saveexec_b64 s[0:1], vcc
	s_cbranch_execz .LBB2_23
	s_mov_b32 s5, 0x5040100
	s_mov_b32 s12, 0
	v_mov_b32_e32 v4, 0
	v_perm_b32 v2, v88, v87, s5
	v_and_b32_e32 v3, 0xffff, v89
	v_mov_b32_e32 v5, v4
	v_mul_u32_u24_e32 v7, 0x150, v0
	s_mov_b32 s13, s12
	ds_write_b128 v7, v[2:5] offset:256
	s_mov_b32 s14, s12
	s_mov_b32 s15, s12
	v_mov_b64_e32 v[2:3], s[12:13]
	v_mov_b64_e32 v[4:5], s[14:15]
	ds_write_b128 v7, v[2:5] offset:272
	ds_write_b128 v7, v[2:5] offset:288
	ds_write_b128 v7, v[2:5] offset:304
